# v2 + combine per-block vector setup loads batched (one wait instead of 10 serialized round trips)
# speedup vs baseline: 1.0210x; 1.0058x over previous
; __device__ __forceinline__ void combine_ln2_phase(Frame& F, int layer) {
;     ...
;     for (int blk = F.vcu; blk < T / 64; blk += F.G) {
;         const int tokb = blk * 64, b = tokb / SEQ;
;         __syncthreads();
;         for (int i = F.tid; i < 1024; i += 512) { PV[i] = modl[(size_t)b * 6144 + 5120 + i] + 1.0f; PV[1024 + i] = lg[i]; PV[2048 + i] = lb[i];
;             if (!lastl) { PV[3072 + i] = modn[(size_t)b * 6144 + 1024 + i] + 1.0f; PV[4096 + i] = modn[(size_t)b * 6144 + i]; } }
;         __syncthreads();
.LBB0_1784:
	s_barrier
	s_and_saveexec_b64 s[0:1], s[40:41]
	s_cbranch_execz .LBB0_1789
	s_ashr_i32 s11, s10, 31
	s_lshr_b32 s11, s11, 27
	s_add_i32 s11, s10, s11
	s_ashr_i32 s11, s11, 5
	s_mul_hi_i32 s22, s11, 0x6000
	s_mulk_i32 s11, 0x6000
	v_readlane_b32 s25, v254, 28
	s_add_u32 s50, s25, s11
	v_readlane_b32 s25, v254, 29
	s_addc_u32 s51, s25, s22
	v_readlane_b32 s25, v254, 30
	s_add_u32 s52, s25, s11
	v_readlane_b32 s25, v254, 31
	s_addc_u32 s53, s25, s22
	v_readlane_b32 s25, v254, 32
	s_add_u32 s54, s25, s11
	v_readlane_b32 s11, v254, 33
	s_addc_u32 s55, s11, s22
	s_mov_b64 s[56:57], 0
	s_mov_b64 s[60:61], s[48:49]
	s_mov_b64 s[62:63], s[46:47]
	s_waitcnt vmcnt(0)
	v_lshl_add_u64 v[6:7], s[50:51], 0, v[36:37]
	global_load_dword v8, v[6:7], off
	global_load_dword v9, v[6:7], off offset:2048
	v_lshl_add_u64 v[6:7], s[60:61], 0, v[36:37]
	global_load_dword v10, v[6:7], off
	global_load_dword v11, v[6:7], off offset:2048
	v_lshl_add_u64 v[6:7], s[62:63], 0, v[36:37]
	global_load_dword v12, v[6:7], off
	global_load_dword v13, v[6:7], off offset:2048
	v_add_u32_e32 v4, 0x800, v82
	s_and_b64 vcc, exec, s[44:45]
	s_cbranch_vccz .Lcpv_last
	v_lshl_add_u64 v[6:7], s[52:53], 0, v[36:37]
	global_load_dword v14, v[6:7], off
	global_load_dword v15, v[6:7], off offset:2048
	v_lshl_add_u64 v[6:7], s[54:55], 0, v[36:37]
	global_load_dword v16, v[6:7], off
	global_load_dword v17, v[6:7], off offset:2048
	s_waitcnt vmcnt(0)
	v_add_f32_e32 v14, 1.0, v14
	v_add_f32_e32 v15, 1.0, v15
	ds_write2st64_b32 v82, v14, v16 offset0:48 offset1:64
	ds_write2st64_b32 v4, v15, v17 offset0:48 offset1:64
.Lcpv_last:
	s_waitcnt vmcnt(0)
	v_add_f32_e32 v8, 1.0, v8
	v_add_f32_e32 v9, 1.0, v9
	ds_write2st64_b32 v82, v8, v10 offset1:16
	ds_write_b32 v82, v12 offset:8192
	ds_write2st64_b32 v4, v9, v11 offset1:16
	ds_write_b32 v4, v13 offset:8192
